# speedup vs baseline: 1.0047x; 1.0034x over previous
_Z7k_protoPKfPf:
	s_load_dwordx4 s[4:7], s[0:1], 0x0
	v_and_b32_e32 v1, 15, v0
	v_lshrrev_b32_e32 v46, 4, v0
	s_lshl_b32 s0, s3, 11
	v_lshl_or_b32 v18, v46, 6, s0
	v_lshlrev_b32_e32 v42, 4, v1
	v_mov_b32_e32 v43, 0
	s_waitcnt lgkmcnt(0)
	v_lshl_add_u64 v[20:21], s[4:5], 0, v[42:43]
	v_ashrrev_i32_e32 v19, 31, v18
	s_mul_i32 s8, s2, 5
	v_lshl_add_u64 v[30:31], v[18:19], 2, v[20:21]
	v_mov_b32_e32 v43, 0x28000
	v_or_b32_e32 v18, 0x400, v18
	v_mad_i64_i32 v[10:11], s[0:1], s8, v43, v[30:31]
	s_add_i32 s4, s8, 1
	s_add_i32 s5, s8, 2
	v_ashrrev_i32_e32 v19, 31, v18
	v_mad_i64_i32 v[12:13], s[0:1], s4, v43, v[30:31]
	global_load_dwordx4 v[2:5], v[10:11], off nt
	global_load_dwordx4 v[6:9], v[12:13], off nt
	v_mad_i64_i32 v[22:23], s[0:1], s5, v43, v[30:31]
	s_add_i32 s9, s8, 3
	v_lshl_add_u64 v[38:39], v[18:19], 2, v[20:21]
	v_mad_i64_i32 v[24:25], s[0:1], s9, v43, v[30:31]
	global_load_dwordx4 v[10:13], v[22:23], off nt
	global_load_dwordx4 v[14:17], v[24:25], off nt
	v_mad_i64_i32 v[18:19], s[0:1], s8, v43, v[38:39]
	v_mad_i64_i32 v[22:23], s[0:1], s4, v43, v[38:39]
	s_add_i32 s10, s8, 4
	global_load_dwordx4 v[18:21], v[18:19], off nt
	v_mad_i64_i32 v[26:27], s[0:1], s5, v43, v[38:39]
	global_load_dwordx4 v[22:25], v[22:23], off nt
	v_mad_i64_i32 v[44:45], s[0:1], s9, v43, v[38:39]
	global_load_dwordx4 v[26:29], v[26:27], off nt
	v_mad_i64_i32 v[40:41], s[0:1], s10, v43, v[30:31]
	global_load_dwordx4 v[30:33], v[44:45], off nt
	global_load_dwordx4 v[34:37], v[40:41], off nt
	v_mad_i64_i32 v[38:39], s[0:1], s10, v43, v[38:39]
	global_load_dwordx4 v[38:41], v[38:39], off nt
	s_movk_i32 s1, 0x120
	s_mov_b32 s0, 0x3e4ccccd
	v_lshrrev_b32_e32 v43, 3, v0
	v_bfe_u32 v44, v0, 4, 2
	v_and_or_b32 v43, v43, 24, v44
	v_lshlrev_b32_e32 v43, 1, v43
	v_mad_u32_u24 v43, v1, s1, v43
	v_cmp_gt_u32_e32 vcc, 64, v0
	s_mul_i32 s4, s2, 20
	v_lshl_or_b32 v42, v46, 8, v42
	s_waitcnt vmcnt(8)
	v_pk_add_f32 v[2:3], v[2:3], v[6:7]
	v_pk_add_f32 v[4:5], v[4:5], v[8:9]
	s_waitcnt vmcnt(7)
	v_pk_add_f32 v[2:3], v[2:3], v[10:11]
	s_waitcnt vmcnt(6)
	v_pk_add_f32 v[2:3], v[2:3], v[14:15]
	v_pk_add_f32 v[4:5], v[4:5], v[12:13]
	s_waitcnt vmcnt(4)
	v_pk_add_f32 v[8:9], v[18:19], v[22:23]
	v_pk_add_f32 v[6:7], v[20:21], v[24:25]
	v_pk_add_f32 v[4:5], v[4:5], v[16:17]
	s_waitcnt vmcnt(3)
	v_pk_add_f32 v[8:9], v[8:9], v[26:27]
	v_pk_add_f32 v[6:7], v[6:7], v[28:29]
	s_waitcnt vmcnt(2)
	v_pk_add_f32 v[8:9], v[8:9], v[30:31]
	s_waitcnt vmcnt(1)
	v_pk_add_f32 v[2:3], v[2:3], v[34:35]
	v_pk_add_f32 v[6:7], v[6:7], v[32:33]
	v_pk_mul_f32 v[2:3], v[2:3], s[0:1] op_sel_hi:[1,0]
	s_waitcnt vmcnt(0)
	v_pk_add_f32 v[8:9], v[8:9], v[38:39]
	v_cvt_f16_f32_e32 v10, v2
	v_pk_add_f32 v[4:5], v[4:5], v[36:37]
	v_pk_add_f32 v[6:7], v[6:7], v[40:41]
	v_pk_mul_f32 v[8:9], v[8:9], s[0:1] op_sel_hi:[1,0]
	v_cvt_f16_f32_e32 v11, v3
	v_pk_mul_f32 v[4:5], v[4:5], s[0:1] op_sel_hi:[1,0]
	v_pk_mul_f32 v[6:7], v[6:7], s[0:1] op_sel_hi:[1,0]
	v_cvt_f16_f32_e32 v12, v8
	v_cvt_f16_f32_e32 v13, v9
	v_pk_mul_f32 v[8:9], v[8:9], v[8:9]
	v_cvt_f16_f32_e32 v14, v4
	v_cvt_f16_f32_e32 v16, v6
	v_cvt_f16_f32_e32 v17, v7
	v_pk_mul_f32 v[6:7], v[6:7], v[6:7]
	v_cvt_f16_f32_e32 v15, v5
	v_pk_fma_f32 v[2:3], v[2:3], v[2:3], v[8:9]
	v_pk_fma_f32 v[4:5], v[4:5], v[4:5], v[6:7]
	ds_write_b16 v43, v10
	ds_write_b16 v43, v11 offset:72
	ds_write_b16 v43, v12 offset:8
	ds_write_b16 v43, v14 offset:144
	ds_write_b16 v43, v15 offset:216
	ds_write_b16 v43, v17 offset:224
	ds_write_b16 v43, v13 offset:80
	ds_write_b16 v43, v16 offset:152
	ds_write_b128 v42, v[2:5] offset:4608
	s_waitcnt lgkmcnt(0)
	s_barrier
	s_mul_hi_i32 s1, s2, 20
	s_ashr_i32 s2, s3, 31
	v_lshrrev_b32_e32 v23, 2, v0
	s_add_u32 s0, s4, s3
	v_and_b32_e32 v23, 48, v23
	s_addc_u32 s1, s1, s2
	v_and_b32_e32 v22, 63, v0
	v_mul_u32_u24_e32 v23, 0x48, v23
	v_mul_u32_u24_e32 v21, 0x48, v1
	v_and_b32_e32 v24, 48, v0
	s_lshl_b64 s[0:1], s[0:1], 8
	v_and_b32_e32 v20, 0xc0, v0
	v_add3_u32 v23, v23, v21, v24
	v_or3_b32 v20, s0, v20, v22
	v_mov_b32_e32 v21, s1
	s_add_u32 s8, s6, 0x32000
	s_addc_u32 s9, s7, 0
	ds_read2_b64 v[26:29], v23 offset1:1
	v_lshl_add_u64 v[24:25], v[20:21], 4, s[8:9]
	s_waitcnt lgkmcnt(0)
	global_store_dwordx4 v[24:25], v[26:29], off
	s_and_saveexec_b64 s[0:1], vcc
	s_cbranch_execz .LBB0_2
	v_lshlrev_b32_e32 v12, 2, v0
	ds_read2st64_b32 v[2:3], v12 offset0:18 offset1:19
	ds_read2st64_b32 v[4:5], v12 offset0:20 offset1:21
	ds_read2st64_b32 v[6:7], v12 offset0:22 offset1:23
	ds_read2st64_b32 v[8:9], v12 offset0:24 offset1:25
	ds_read2st64_b32 v[10:11], v12 offset0:26 offset1:27
	s_waitcnt lgkmcnt(4)
	v_add_f32_e32 v2, 0, v2
	v_add_f32_e32 v2, v2, v3
	s_waitcnt lgkmcnt(3)
	v_add_f32_e32 v2, v2, v4
	v_add_f32_e32 v2, v2, v5
	s_waitcnt lgkmcnt(2)
	v_add_f32_e32 v2, v2, v6
	v_add_f32_e32 v2, v2, v7
	s_waitcnt lgkmcnt(1)
	v_add_f32_e32 v2, v2, v8
	v_add_f32_e32 v8, v2, v9
	ds_read2st64_b32 v[2:3], v12 offset0:28 offset1:29
	ds_read2st64_b32 v[4:5], v12 offset0:30 offset1:31
	ds_read2st64_b32 v[6:7], v12 offset0:32 offset1:33
	s_waitcnt lgkmcnt(3)
	v_add_f32_e32 v8, v8, v10
	v_add_f32_e32 v8, v8, v11
	s_waitcnt lgkmcnt(2)
	v_add_f32_e32 v2, v8, v2
	v_add_f32_e32 v2, v2, v3
	s_waitcnt lgkmcnt(1)
	v_add_f32_e32 v2, v2, v4
	v_add_f32_e32 v2, v2, v5
	s_waitcnt lgkmcnt(0)
	v_add_f32_e32 v2, v2, v6
	s_add_i32 s5, s4, s3
	v_add_f32_e32 v4, v2, v7
	v_lshl_or_b32 v2, s5, 6, v0
	v_ashrrev_i32_e32 v3, 31, v2
	v_lshl_add_u64 v[2:3], v[2:3], 2, s[6:7]
	global_store_dword v[2:3], v4, off
